# speedup vs baseline: 1.0372x; 1.0038x over previous
.LBB2_1:
	s_add_i32 s13, s3, -4
	s_and_b32 s13, s13, 4
	s_mulk_i32 s13, 0x2400
	v_add_u32_e32 v124, s13, v120
	ds_read_b128 v[96:99], v124
	ds_read_b128 v[126:129], v124 offset:32
	ds_read_b128 v[130:133], v124 offset:4608
	ds_read_b128 v[134:137], v124 offset:4640
	v_lshl_add_u64 v[118:119], v[108:109], 0, s[4:5]
	v_add_co_u32_e32 v150, vcc, s12, v118
	s_waitcnt vmcnt(7) lgkmcnt(3)
	v_mfma_f32_32x32x16_f16 v[48:63], v[96:99], v[88:91], 0
	v_mov_b32_e32 v125, v116
	v_lshl_add_u64 v[116:117], v[110:111], 0, s[4:5]
	v_addc_co_u32_e32 v151, vcc, 0, v119, vcc
	v_mov_b32_e32 v123, v100
	v_lshl_add_u64 v[102:103], v[112:113], 0, s[6:7]
	v_lshl_add_u64 v[100:101], v[114:115], 0, s[6:7]
	s_waitcnt lgkmcnt(1)
	v_mfma_f32_32x32x16_f16 v[32:47], v[130:133], v[88:91], 0
	v_add_co_u32_e32 v158, vcc, s12, v116
	s_and_b32 s13, s3, 4
	s_nop 0
	v_addc_co_u32_e32 v159, vcc, 0, v117, vcc
	s_mulk_i32 s13, 0x2400
	v_add_u32_e32 v218, s13, v121
	s_waitcnt vmcnt(5)
	v_mfma_f32_32x32x16_f16 v[48:63], v[96:99], v[92:95], v[48:63]
	s_add_u32 s6, s6, 0x80
	s_addc_u32 s7, s7, 0
	s_add_i32 s3, s3, 4
	s_add_u32 s4, s4, 0x2000
	s_addc_u32 s5, s5, 0
	s_cmpk_eq_i32 s6, 0x780
	v_mfma_f32_32x32x16_f16 v[32:47], v[130:133], v[92:95], v[32:47]
	ds_read_b128 v[96:99], v124 offset:9216
	ds_read_b128 v[130:133], v124 offset:9248
	s_waitcnt lgkmcnt(1)
	v_mfma_f32_32x32x16_f16 v[48:63], v[96:99], v[88:91], v[48:63]
	ds_read_b128 v[138:141], v124 offset:13824
	ds_read_b128 v[96:99], v124 offset:13856
	s_waitcnt lgkmcnt(1)
	v_mfma_f32_32x32x16_f16 v[32:47], v[138:141], v[88:91], v[32:47]
	v_mfma_f32_32x32x16_f16 v[48:63], v[126:129], v[80:83], v[48:63]
	v_mfma_f32_32x32x16_f16 v[32:47], v[134:137], v[80:83], v[32:47]
	s_waitcnt vmcnt(4)
	v_mfma_f32_32x32x16_f16 v[48:63], v[126:129], v[84:87], v[48:63]
	v_mfma_f32_32x32x16_f16 v[32:47], v[134:137], v[84:87], v[32:47]
	v_mfma_f32_32x32x16_f16 v[48:63], v[130:133], v[80:83], v[48:63]
	s_waitcnt lgkmcnt(0)
	v_mfma_f32_32x32x16_f16 v[32:47], v[96:99], v[80:83], v[32:47]
	ds_read_b128 v[96:99], v124 offset:64
	ds_read_b128 v[126:129], v124 offset:96
	ds_read_b128 v[130:133], v124 offset:4672
	ds_read_b128 v[134:137], v124 offset:4704
	global_load_dwordx4 v[116:119], v[102:103], off offset:128
	global_load_dwordx4 v[138:141], v[100:101], off offset:128
	v_add_co_u32_e32 v102, vcc, s1, v102
	s_waitcnt vmcnt(5) lgkmcnt(3)
	v_mfma_f32_32x32x16_f16 v[48:63], v[96:99], v[72:75], v[48:63]
	v_addc_co_u32_e32 v103, vcc, 0, v103, vcc
	v_add_co_u32_e32 v100, vcc, s1, v100
	s_nop 1
	v_addc_co_u32_e32 v101, vcc, 0, v101, vcc
	s_waitcnt lgkmcnt(1)
	v_mfma_f32_32x32x16_f16 v[32:47], v[130:133], v[72:75], v[32:47]
	s_waitcnt vmcnt(3)
	v_mfma_f32_32x32x16_f16 v[48:63], v[96:99], v[76:79], v[48:63]
	v_mfma_f32_32x32x16_f16 v[32:47], v[130:133], v[76:79], v[32:47]
	ds_read_b128 v[96:99], v124 offset:9280
	ds_read_b128 v[130:133], v124 offset:9312
	s_waitcnt lgkmcnt(1)
	v_mfma_f32_32x32x16_f16 v[48:63], v[96:99], v[72:75], v[48:63]
	ds_read_b128 v[96:99], v124 offset:13888
	ds_read_b128 v[142:145], v124 offset:13920
	global_load_dwordx4 v[146:149], v[150:151], off offset:-4096
	s_nop 0
	global_load_dwordx4 v[150:153], v[150:151], off
	s_nop 0
	global_load_dwordx4 v[154:157], v[158:159], off offset:-4096
	s_nop 0
	global_load_dwordx4 v[158:161], v[158:159], off
	s_nop 0
	global_load_dwordx4 v[162:165], v[102:103], off offset:128
	global_load_dwordx4 v[166:169], v[100:101], off offset:128
	ds_read_b128 v[170:173], v124 offset:23040
	ds_read_b128 v[174:177], v124 offset:18432
	ds_read_b128 v[178:181], v124 offset:18464
	ds_read_b128 v[182:185], v124 offset:27648
	ds_read_b128 v[186:189], v124 offset:27680
	v_mfma_f32_32x32x16_f16 v[48:63], v[126:129], v[64:67], v[48:63]
	s_waitcnt lgkmcnt(6)
	v_mfma_f32_32x32x16_f16 v[32:47], v[96:99], v[72:75], v[32:47]
	s_waitcnt vmcnt(8)
	v_mfma_f32_32x32x16_f16 v[48:63], v[126:129], v[68:71], v[48:63]
	ds_read_b128 v[126:129], v124 offset:23072
	ds_read_b128 v[190:193], v124 offset:32256
	ds_read_b128 v[194:197], v124 offset:32288
	ds_read_b128 v[198:201], v124 offset:18496
	ds_read_b128 v[202:205], v124 offset:18528
	ds_read_b128 v[206:209], v124 offset:27712
	ds_read_b128 v[100:103], v124 offset:27744
	v_mfma_f32_32x32x16_f16 v[32:47], v[134:137], v[64:67], v[32:47]
	v_mfma_f32_32x32x16_f16 v[48:63], v[130:133], v[64:67], v[48:63]
	v_mfma_f32_32x32x16_f16 v[32:47], v[134:137], v[68:71], v[32:47]
	ds_read_b128 v[134:137], v124 offset:23104
	ds_read_b128 v[210:213], v124 offset:23136
	ds_read_b128 v[214:217], v124 offset:32320
	ds_read_b128 v[96:99], v124 offset:32352
	s_waitcnt vmcnt(7)
	ds_write_b128 v218, v[116:119] offset:18432
	s_waitcnt vmcnt(6)
	ds_write_b128 v218, v[138:141] offset:27648
	s_waitcnt vmcnt(5)
	ds_write_b128 v218, v[146:149]
	s_waitcnt vmcnt(4)
	ds_write_b128 v218, v[150:153] offset:4608
	s_waitcnt vmcnt(3)
	ds_write_b128 v218, v[154:157] offset:9216
	s_waitcnt vmcnt(2)
	ds_write_b128 v218, v[158:161] offset:13824
	s_waitcnt vmcnt(1)
	ds_write_b128 v218, v[162:165] offset:23040
	v_max_f32_e32 v116, v49, v49
	v_max_f32_e32 v117, v48, v48
	s_waitcnt lgkmcnt(14)
	v_mfma_f32_32x32x16_f16 v[32:47], v[142:145], v[64:67], v[32:47]
	v_max_f32_e32 v116, v117, v116
	v_max3_f32 v116, v116, v50, v51
	v_max3_f32 v116, v116, v52, v53
	v_max3_f32 v116, v116, v54, v55
	v_max3_f32 v116, v116, v56, v57
	v_max3_f32 v116, v116, v58, v59
	v_max3_f32 v116, v116, v60, v61
	v_max3_f32 v116, v116, v62, v63
	s_nop 3
	v_max3_f32 v116, v116, v32, v33
	v_max3_f32 v116, v116, v34, v35
	v_max3_f32 v116, v116, v36, v37
	v_max3_f32 v116, v116, v38, v39
	v_max3_f32 v116, v116, v40, v41
	v_max3_f32 v116, v116, v42, v43
	v_max3_f32 v116, v116, v44, v45
	v_max3_f32 v116, v116, v46, v47
	ds_bpermute_b32 v117, v107, v116
	s_waitcnt vmcnt(0)
	ds_write_b128 v218, v[166:169] offset:32256
	s_waitcnt lgkmcnt(0)
	s_barrier
	v_max3_f32 v116, v125, v116, v117
	v_sub_f32_e32 v117, v125, v116
	v_fmamk_f32 v119, v116, 0xb9b8aa3b, v122
	v_mul_f32_e32 v117, 0x39b8aa3b, v117
	v_fmamk_f32 v48, v48, 0x39b8aa3b, v119
	v_fmamk_f32 v49, v49, 0x39b8aa3b, v119
	v_fmamk_f32 v50, v50, 0x39b8aa3b, v119
	v_fmamk_f32 v51, v51, 0x39b8aa3b, v119
	v_fmamk_f32 v52, v52, 0x39b8aa3b, v119
	v_fmamk_f32 v53, v53, 0x39b8aa3b, v119
	v_fmamk_f32 v54, v54, 0x39b8aa3b, v119
	v_fmamk_f32 v55, v55, 0x39b8aa3b, v119
	v_exp_f32_e32 v118, v117
	v_exp_f32_e32 v117, v48
	v_exp_f32_e32 v140, v49
	v_exp_f32_e32 v124, v50
	v_exp_f32_e32 v125, v51
	v_exp_f32_e32 v130, v52
	v_exp_f32_e32 v131, v53
	v_exp_f32_e32 v132, v54
	v_exp_f32_e32 v133, v55
	v_cvt_f16_f32_e32 v141, v117
	v_cvt_f16_f32_e32 v142, v140
	v_mul_f32_e32 v30, v118, v30
	v_mul_f32_e32 v31, v118, v31
	v_mul_f32_e32 v28, v118, v28
	v_mul_f32_e32 v29, v118, v29
	v_mul_f32_e32 v26, v118, v26
	v_mul_f32_e32 v27, v118, v27
	v_mul_f32_e32 v24, v118, v24
	v_mul_f32_e32 v25, v118, v25
	v_mul_f32_e32 v22, v118, v22
	v_mul_f32_e32 v23, v118, v23
	v_mul_f32_e32 v20, v118, v20
	v_mul_f32_e32 v21, v118, v21
	v_mul_f32_e32 v18, v118, v18
	v_mul_f32_e32 v19, v118, v19
	v_mul_f32_e32 v16, v118, v16
	v_mul_f32_e32 v17, v118, v17
	v_mul_f32_e32 v14, v118, v14
	v_mul_f32_e32 v15, v118, v15
	v_mul_f32_e32 v12, v118, v12
	v_mul_f32_e32 v13, v118, v13
	v_mul_f32_e32 v10, v118, v10
	v_mul_f32_e32 v11, v118, v11
	v_mul_f32_e32 v8, v118, v8
	v_mul_f32_e32 v9, v118, v9
	v_mul_f32_e32 v6, v118, v6
	v_mul_f32_e32 v7, v118, v7
	v_mul_f32_e32 v4, v118, v4
	v_mul_f32_e32 v5, v118, v5
	v_mul_f32_e32 v2, v118, v2
	v_mul_f32_e32 v3, v118, v3
	v_mul_f32_e32 v0, v118, v0
	v_mul_f32_e32 v1, v118, v1
	v_cvt_pk_f16_f32 v48, v117, v140
	v_cvt_pk_f16_f32 v49, v124, v125
	v_cvt_pk_f16_f32 v50, v130, v131
	v_cvt_pk_f16_f32 v51, v132, v133
	v_cvt_f32_f16_e32 v52, v49
	v_cvt_f32_f16_sdwa v53, v49 dst_sel:DWORD dst_unused:UNUSED_PAD src0_sel:WORD_1
	v_mfma_f32_32x32x16_f16 v[16:31], v[174:177], v[48:51], v[16:31]
	v_cvt_f32_f16_e32 v54, v50
	v_cvt_f32_f16_sdwa v55, v50 dst_sel:DWORD dst_unused:UNUSED_PAD src0_sel:WORD_1
	v_cvt_f32_f16_e32 v138, v51
	v_cvt_f32_f16_sdwa v139, v51 dst_sel:DWORD dst_unused:UNUSED_PAD src0_sel:WORD_1
	v_cvt_f32_f16_e32 v141, v141
	v_cvt_f32_f16_e32 v142, v142
	v_sub_f32_e32 v52, v124, v52
	v_sub_f32_e32 v53, v125, v53
	v_mfma_f32_32x32x16_f16 v[0:15], v[170:173], v[48:51], v[0:15]
	v_add_f32_e64 v54, v130, -v54
	v_add_f32_e64 v55, v131, -v55
	v_add_f32_e64 v138, v132, -v138
	v_add_f32_e64 v139, v133, -v139
	v_cvt_pk_f16_f32 v53, v52, v53
	v_cvt_pk_f16_f32 v54, v54, v55
	v_cvt_pk_f16_f32 v55, v138, v139
	v_sub_f32_e32 v52, v117, v141
	v_sub_f32_e32 v138, v140, v142
	v_cvt_pk_f16_f32 v52, v52, v138
	v_fmamk_f32 v56, v56, 0x39b8aa3b, v119
	v_fmamk_f32 v57, v57, 0x39b8aa3b, v119
	v_mfma_f32_32x32x16_f16 v[16:31], v[174:177], v[52:55], v[16:31]
	v_fmamk_f32 v58, v58, 0x39b8aa3b, v119
	v_fmamk_f32 v59, v59, 0x39b8aa3b, v119
	v_exp_f32_e32 v138, v56
	v_exp_f32_e32 v139, v57
	v_exp_f32_e32 v56, v58
	v_exp_f32_e32 v57, v59
	v_cvt_f16_f32_e32 v141, v138
	v_mfma_f32_32x32x16_f16 v[0:15], v[170:173], v[52:55], v[0:15]
	v_fmamk_f32 v52, v60, 0x39b8aa3b, v119
	v_fmamk_f32 v53, v61, 0x39b8aa3b, v119
	v_fmamk_f32 v54, v62, 0x39b8aa3b, v119
	v_fmamk_f32 v55, v63, 0x39b8aa3b, v119
	v_exp_f32_e32 v58, v52
	v_exp_f32_e32 v59, v53
	v_exp_f32_e32 v60, v54
	v_mfma_f32_32x32x16_f16 v[16:31], v[182:185], v[48:51], v[16:31]
	v_exp_f32_e32 v61, v55
	v_cvt_f16_f32_e32 v142, v139
	v_cvt_f32_f16_e32 v141, v141
	v_fmamk_f32 v32, v32, 0x39b8aa3b, v119
	v_fmamk_f32 v33, v33, 0x39b8aa3b, v119
	v_cvt_f32_f16_e32 v142, v142
	v_fmamk_f32 v34, v34, 0x39b8aa3b, v119
	v_mfma_f32_32x32x16_f16 v[0:15], v[190:193], v[48:51], v[0:15]
	v_cvt_pk_f16_f32 v48, v138, v139
	v_cvt_pk_f16_f32 v49, v56, v57
	v_cvt_pk_f16_f32 v50, v58, v59
	v_cvt_pk_f16_f32 v51, v60, v61
	v_cvt_f32_f16_e32 v52, v49
	v_cvt_f32_f16_sdwa v53, v49 dst_sel:DWORD dst_unused:UNUSED_PAD src0_sel:WORD_1
	v_cvt_f32_f16_e32 v54, v50
	v_mfma_f32_32x32x16_f16 v[16:31], v[178:181], v[48:51], v[16:31]
	v_cvt_f32_f16_sdwa v55, v50 dst_sel:DWORD dst_unused:UNUSED_PAD src0_sel:WORD_1
	v_cvt_f32_f16_e32 v62, v51
	v_cvt_f32_f16_sdwa v63, v51 dst_sel:DWORD dst_unused:UNUSED_PAD src0_sel:WORD_1
	v_add_f32_e64 v52, v56, -v52
	v_add_f32_e64 v53, v57, -v53
	v_sub_f32_e32 v54, v58, v54
	v_sub_f32_e32 v55, v59, v55
	v_cvt_pk_f16_f32 v53, v52, v53
	v_sub_f32_e32 v62, v60, v62
	v_sub_f32_e32 v63, v61, v63
	v_mfma_f32_32x32x16_f16 v[0:15], v[126:129], v[48:51], v[0:15]
	v_cvt_pk_f16_f32 v54, v54, v55
	v_cvt_pk_f16_f32 v55, v62, v63
	v_sub_f32_e32 v52, v138, v141
	v_sub_f32_e32 v62, v139, v142
	v_cvt_pk_f16_f32 v52, v52, v62
	v_fmamk_f32 v35, v35, 0x39b8aa3b, v119
	v_fmamk_f32 v36, v36, 0x39b8aa3b, v119
	v_mfma_f32_32x32x16_f16 v[16:31], v[178:181], v[52:55], v[16:31]
	v_fmamk_f32 v37, v37, 0x39b8aa3b, v119
	v_fmamk_f32 v38, v38, 0x39b8aa3b, v119
	v_fmamk_f32 v39, v39, 0x39b8aa3b, v119
	v_fmamk_f32 v62, v40, 0x39b8aa3b, v119
	v_fmamk_f32 v63, v41, 0x39b8aa3b, v119
	v_exp_f32_e32 v40, v34
	v_exp_f32_e32 v41, v35
	v_mfma_f32_32x32x16_f16 v[0:15], v[126:129], v[52:55], v[0:15]
	v_exp_f32_e32 v126, v32
	v_exp_f32_e32 v127, v33
	v_exp_f32_e32 v52, v36
	v_exp_f32_e32 v53, v37
	v_exp_f32_e32 v54, v38
	v_exp_f32_e32 v55, v39
	v_cvt_f16_f32_e32 v128, v126
	v_mfma_f32_32x32x16_f16 v[16:31], v[186:189], v[48:51], v[16:31]
	v_cvt_f16_f32_e32 v129, v127
	v_cvt_pk_f16_f32 v32, v126, v127
	v_cvt_pk_f16_f32 v33, v40, v41
	v_cvt_pk_f16_f32 v34, v52, v53
	v_cvt_pk_f16_f32 v35, v54, v55
	v_cvt_f32_f16_e32 v36, v33
	v_cvt_f32_f16_sdwa v37, v33 dst_sel:DWORD dst_unused:UNUSED_PAD src0_sel:WORD_1
	v_mfma_f32_32x32x16_f16 v[0:15], v[194:197], v[48:51], v[0:15]
	v_cvt_f32_f16_e32 v38, v34
	v_cvt_f32_f16_sdwa v39, v34 dst_sel:DWORD dst_unused:UNUSED_PAD src0_sel:WORD_1
	v_cvt_f32_f16_e32 v48, v35
	v_cvt_f32_f16_sdwa v49, v35 dst_sel:DWORD dst_unused:UNUSED_PAD src0_sel:WORD_1
	v_cvt_f32_f16_e32 v50, v128
	v_cvt_f32_f16_e32 v51, v129
	v_sub_f32_e32 v36, v40, v36
	v_sub_f32_e32 v37, v41, v37
	v_mfma_f32_32x32x16_f16 v[16:31], v[198:201], v[32:35], v[16:31]
	v_add_f32_e64 v38, v52, -v38
	v_add_f32_e64 v39, v53, -v39
	v_add_f32_e64 v48, v54, -v48
	v_add_f32_e64 v49, v55, -v49
	v_cvt_pk_f16_f32 v37, v36, v37
	v_cvt_pk_f16_f32 v38, v38, v39
	v_cvt_pk_f16_f32 v39, v48, v49
	v_sub_f32_e32 v36, v126, v50
	v_sub_f32_e32 v48, v127, v51
	v_mfma_f32_32x32x16_f16 v[0:15], v[134:137], v[32:35], v[0:15]
	v_cvt_pk_f16_f32 v36, v36, v48
	v_exp_f32_e32 v50, v62
	v_exp_f32_e32 v51, v63
	v_fmamk_f32 v42, v42, 0x39b8aa3b, v119
	v_fmamk_f32 v43, v43, 0x39b8aa3b, v119
	v_fmamk_f32 v44, v44, 0x39b8aa3b, v119
	v_fmamk_f32 v45, v45, 0x39b8aa3b, v119
	v_mfma_f32_32x32x16_f16 v[16:31], v[198:201], v[36:39], v[16:31]
	v_fmamk_f32 v46, v46, 0x39b8aa3b, v119
	v_fmac_f32_e32 v119, 0x39b8aa3b, v47
	v_exp_f32_e32 v42, v42
	v_exp_f32_e32 v43, v43
	v_exp_f32_e32 v44, v44
	v_exp_f32_e32 v45, v45
	v_exp_f32_e32 v46, v46
	v_mfma_f32_32x32x16_f16 v[0:15], v[134:137], v[36:39], v[0:15]
	v_exp_f32_e32 v47, v119
	v_cvt_f16_f32_e32 v62, v50
	v_cvt_f16_f32_e32 v63, v51
	v_add_f32_e32 v48, 0, v117
	v_cvt_pk_f16_f32 v37, v42, v43
	v_cvt_pk_f16_f32 v38, v44, v45
	v_cvt_pk_f16_f32 v39, v46, v47
	v_mfma_f32_32x32x16_f16 v[16:31], v[206:209], v[32:35], v[16:31]
	v_add_f32_e32 v117, v48, v140
	v_cvt_f32_f16_e32 v48, v39
	v_cvt_f32_f16_sdwa v49, v39 dst_sel:DWORD dst_unused:UNUSED_PAD src0_sel:WORD_1
	v_cvt_f32_f16_e32 v62, v62
	v_cvt_f32_f16_e32 v63, v63
	v_add_f32_e32 v117, v117, v124
	v_cvt_pk_f16_f32 v36, v50, v51
	v_mfma_f32_32x32x16_f16 v[0:15], v[214:217], v[32:35], v[0:15]
	v_cvt_f32_f16_e32 v32, v37
	v_cvt_f32_f16_sdwa v33, v37 dst_sel:DWORD dst_unused:UNUSED_PAD src0_sel:WORD_1
	v_cvt_f32_f16_e32 v34, v38
	v_cvt_f32_f16_sdwa v35, v38 dst_sel:DWORD dst_unused:UNUSED_PAD src0_sel:WORD_1
	v_add_f32_e32 v117, v117, v125
	v_sub_f32_e32 v32, v42, v32
	v_sub_f32_e32 v33, v43, v33
	v_sub_f32_e32 v48, v46, v48
	v_sub_f32_e32 v49, v47, v49
	v_sub_f32_e32 v34, v44, v34
	v_sub_f32_e32 v35, v45, v35
	v_mfma_f32_32x32x16_f16 v[16:31], v[202:205], v[36:39], v[16:31]
	v_add_f32_e32 v117, v117, v130
	v_cvt_pk_f16_f32 v33, v32, v33
	v_cvt_pk_f16_f32 v34, v34, v35
	v_cvt_pk_f16_f32 v35, v48, v49
	v_sub_f32_e32 v32, v50, v62
	v_sub_f32_e32 v48, v51, v63
	v_cvt_pk_f16_f32 v32, v32, v48
	v_mfma_f32_32x32x16_f16 v[0:15], v[210:213], v[36:39], v[0:15]
	v_add_f32_e32 v48, v117, v131
	v_add_f32_e32 v48, v48, v132
	v_add_f32_e32 v48, v48, v133
	v_add_f32_e32 v48, v48, v138
	v_add_f32_e32 v48, v48, v139
	v_add_f32_e32 v48, v48, v56
	v_add_f32_e32 v48, v48, v57
	v_mfma_f32_32x32x16_f16 v[16:31], v[202:205], v[32:35], v[16:31]
	v_mfma_f32_32x32x16_f16 v[0:15], v[210:213], v[32:35], v[0:15]
	v_add_f32_e32 v32, v48, v58
	v_add_f32_e32 v32, v32, v59
	v_add_f32_e32 v32, v32, v60
	v_add_f32_e32 v32, v32, v61
	v_add_f32_e32 v32, v32, v126
	v_add_f32_e32 v32, v32, v127
	v_add_f32_e32 v32, v32, v40
	v_add_f32_e32 v32, v32, v41
	v_add_f32_e32 v32, v32, v52
	v_add_f32_e32 v32, v32, v53
	v_add_f32_e32 v32, v32, v54
	v_add_f32_e32 v32, v32, v55
	v_add_f32_e32 v32, v32, v50
	v_mfma_f32_32x32x16_f16 v[16:31], v[100:103], v[36:39], v[16:31]
	v_add_f32_e32 v32, v32, v51
	v_add_f32_e32 v32, v32, v42
	v_add_f32_e32 v32, v32, v43
	v_add_f32_e32 v32, v32, v44
	v_add_f32_e32 v32, v32, v45
	v_add_f32_e32 v32, v32, v46
	v_add_f32_e32 v100, v32, v47
	v_mfma_f32_32x32x16_f16 v[0:15], v[96:99], v[36:39], v[0:15]
	v_fmac_f32_e32 v100, v123, v118
	s_cbranch_scc0 .LBB2_1
	ds_read_b128 v[48:51], v120 offset:36864
	ds_read_b128 v[52:55], v120 offset:36896
	v_add_u32_e32 v102, 0xea00, v120
	s_ashr_i32 s0, s0, 3
	s_ashr_i32 s1, s0, 31
	s_waitcnt lgkmcnt(1)
	v_mfma_f32_32x32x16_f16 v[32:47], v[48:51], v[88:91], 0
	s_lshl_b64 s[0:1], s[0:1], 10
	v_mfma_f32_32x32x16_f16 v[32:47], v[48:51], v[92:95], v[32:47]
	ds_read_b128 v[48:51], v120 offset:46080
	ds_read_b128 v[56:59], v120 offset:46112
	s_waitcnt lgkmcnt(1)
	v_mfma_f32_32x32x16_f16 v[32:47], v[48:51], v[88:91], v[32:47]
	v_mfma_f32_32x32x16_f16 v[32:47], v[52:55], v[80:83], v[32:47]
	v_mfma_f32_32x32x16_f16 v[32:47], v[52:55], v[84:87], v[32:47]
	ds_read_b128 v[48:51], v120 offset:36928
	ds_read_b128 v[52:55], v120 offset:36960
	s_waitcnt lgkmcnt(2)
	v_mfma_f32_32x32x16_f16 v[32:47], v[56:59], v[80:83], v[32:47]
	s_waitcnt lgkmcnt(1)
	v_mfma_f32_32x32x16_f16 v[32:47], v[48:51], v[72:75], v[32:47]
	v_mfma_f32_32x32x16_f16 v[32:47], v[48:51], v[76:79], v[32:47]
	ds_read_b128 v[48:51], v120 offset:46144
	ds_read_b128 v[56:59], v120 offset:46176
	ds_read_b128 v[96:99], v120 offset:41472
	ds_read_b128 v[108:111], v120 offset:41504
	s_waitcnt lgkmcnt(3)
	v_mfma_f32_32x32x16_f16 v[32:47], v[48:51], v[72:75], v[32:47]
	v_mfma_f32_32x32x16_f16 v[32:47], v[52:55], v[64:67], v[32:47]
	v_mfma_f32_32x32x16_f16 v[32:47], v[52:55], v[68:71], v[32:47]
	s_waitcnt lgkmcnt(2)
	v_mfma_f32_32x32x16_f16 v[32:47], v[56:59], v[64:67], v[32:47]
	s_waitcnt lgkmcnt(1)
	v_mfma_f32_32x32x16_f16 v[48:63], v[96:99], v[88:91], 0
	v_mfma_f32_32x32x16_f16 v[48:63], v[96:99], v[92:95], v[48:63]
	ds_read_b128 v[92:95], v120 offset:50688
	ds_read_b128 v[96:99], v120 offset:50720
	s_waitcnt lgkmcnt(1)
	v_mfma_f32_32x32x16_f16 v[48:63], v[92:95], v[88:91], v[48:63]
	v_mfma_f32_32x32x16_f16 v[48:63], v[108:111], v[80:83], v[48:63]
	v_mfma_f32_32x32x16_f16 v[48:63], v[108:111], v[84:87], v[48:63]
	s_waitcnt lgkmcnt(0)
	v_mfma_f32_32x32x16_f16 v[48:63], v[96:99], v[80:83], v[48:63]
	ds_read_b128 v[80:83], v120 offset:41536
	ds_read_b128 v[84:87], v120 offset:41568
	s_waitcnt lgkmcnt(1)
	v_mfma_f32_32x32x16_f16 v[48:63], v[80:83], v[72:75], v[48:63]
	v_mfma_f32_32x32x16_f16 v[48:63], v[80:83], v[76:79], v[48:63]
	ds_read_b128 v[76:79], v120 offset:50752
	ds_read_b128 v[80:83], v120 offset:50784
	s_waitcnt lgkmcnt(1)
	v_mfma_f32_32x32x16_f16 v[48:63], v[76:79], v[72:75], v[48:63]
	v_max_f32_e32 v72, v33, v33
	v_max_f32_e32 v73, v32, v32
	v_max_f32_e32 v72, v73, v72
	v_mfma_f32_32x32x16_f16 v[48:63], v[84:87], v[64:67], v[48:63]
	v_mfma_f32_32x32x16_f16 v[48:63], v[84:87], v[68:71], v[48:63]
	v_max3_f32 v68, v72, v34, v35
	v_max3_f32 v68, v68, v36, v37
	v_max3_f32 v68, v68, v38, v39
	v_max3_f32 v68, v68, v40, v41
	v_max3_f32 v68, v68, v42, v43
	v_max3_f32 v68, v68, v44, v45
	v_max3_f32 v68, v68, v46, v47
	s_waitcnt lgkmcnt(0)
	v_mfma_f32_32x32x16_f16 v[48:63], v[80:83], v[64:67], v[48:63]
	s_nop 11
	v_max3_f32 v64, v68, v48, v49
	v_max3_f32 v64, v64, v50, v51
	v_max3_f32 v64, v64, v52, v53
	v_max3_f32 v64, v64, v54, v55
	v_max3_f32 v64, v64, v56, v57
	v_max3_f32 v64, v64, v58, v59
	v_max3_f32 v64, v64, v60, v61
	v_max3_f32 v64, v64, v62, v63
	ds_bpermute_b32 v65, v107, v64
	v_mov_b32_e32 v68, 0x41000000
	s_waitcnt lgkmcnt(0)
	v_max3_f32 v65, v116, v64, v65
	v_fmac_f32_e32 v68, 0xb9b8aa3b, v65
	v_fmamk_f32 v32, v32, 0x39b8aa3b, v68
	v_sub_f32_e32 v64, v116, v65
	v_exp_f32_e32 v65, v32
	v_fmamk_f32 v32, v33, 0x39b8aa3b, v68
	v_exp_f32_e32 v101, v32
	v_fmamk_f32 v32, v34, 0x39b8aa3b, v68
	v_exp_f32_e32 v66, v32
	v_fmamk_f32 v32, v35, 0x39b8aa3b, v68
	v_exp_f32_e32 v67, v32
	v_fmamk_f32 v32, v36, 0x39b8aa3b, v68
	v_exp_f32_e32 v36, v32
	v_fmamk_f32 v32, v37, 0x39b8aa3b, v68
	v_exp_f32_e32 v37, v32
	v_fmamk_f32 v32, v38, 0x39b8aa3b, v68
	v_exp_f32_e32 v38, v32
	v_fmamk_f32 v32, v39, 0x39b8aa3b, v68
	v_exp_f32_e32 v39, v32
	v_fmamk_f32 v32, v40, 0x39b8aa3b, v68
	v_exp_f32_e32 v124, v32
	v_fmamk_f32 v32, v41, 0x39b8aa3b, v68
	v_exp_f32_e32 v125, v32
	v_fmamk_f32 v32, v42, 0x39b8aa3b, v68
	v_exp_f32_e32 v40, v32
	v_fmamk_f32 v32, v43, 0x39b8aa3b, v68
	v_exp_f32_e32 v41, v32
	v_fmamk_f32 v32, v44, 0x39b8aa3b, v68
	v_exp_f32_e32 v42, v32
	v_fmamk_f32 v32, v45, 0x39b8aa3b, v68
	v_exp_f32_e32 v43, v32
	v_fmamk_f32 v32, v46, 0x39b8aa3b, v68
	v_exp_f32_e32 v44, v32
	v_fmamk_f32 v32, v47, 0x39b8aa3b, v68
	v_exp_f32_e32 v45, v32
	v_fmamk_f32 v32, v48, 0x39b8aa3b, v68
	v_exp_f32_e32 v126, v32
	v_fmamk_f32 v32, v49, 0x39b8aa3b, v68
	v_exp_f32_e32 v127, v32
	v_fmamk_f32 v32, v50, 0x39b8aa3b, v68
	v_exp_f32_e32 v46, v32
	v_fmamk_f32 v32, v51, 0x39b8aa3b, v68
	v_exp_f32_e32 v47, v32
	v_fmamk_f32 v32, v52, 0x39b8aa3b, v68
	v_exp_f32_e32 v48, v32
	v_fmamk_f32 v32, v53, 0x39b8aa3b, v68
	v_exp_f32_e32 v49, v32
	v_fmamk_f32 v32, v54, 0x39b8aa3b, v68
	v_exp_f32_e32 v50, v32
	v_fmamk_f32 v32, v55, 0x39b8aa3b, v68
	v_exp_f32_e32 v51, v32
	v_fmamk_f32 v32, v56, 0x39b8aa3b, v68
	v_exp_f32_e32 v128, v32
	v_fmamk_f32 v32, v57, 0x39b8aa3b, v68
	v_exp_f32_e32 v129, v32
	v_fmamk_f32 v32, v58, 0x39b8aa3b, v68
	v_exp_f32_e32 v52, v32
	v_fmamk_f32 v32, v59, 0x39b8aa3b, v68
	v_exp_f32_e32 v53, v32
	v_fmamk_f32 v32, v60, 0x39b8aa3b, v68
	v_exp_f32_e32 v54, v32
	v_fmamk_f32 v32, v61, 0x39b8aa3b, v68
	v_exp_f32_e32 v55, v32
	v_fmamk_f32 v32, v62, 0x39b8aa3b, v68
	v_exp_f32_e32 v56, v32
	v_cvt_f16_f32_e32 v32, v65
	v_cvt_f16_f32_e32 v33, v101
	v_cvt_pk_f16_f32 v59, v66, v67
	v_cvt_pk_f16_f32 v60, v36, v37
	v_cvt_f32_f16_e32 v32, v32
	v_cvt_f32_f16_e32 v35, v33
	v_cvt_f32_f16_sdwa v33, v59 dst_sel:DWORD dst_unused:UNUSED_PAD src0_sel:WORD_1
	v_fmac_f32_e32 v68, 0x39b8aa3b, v63
	v_sub_f32_e32 v34, v65, v32
	v_cvt_f32_f16_e32 v32, v59
	v_sub_f32_e32 v35, v101, v35
	v_cvt_pk_f16_f32 v61, v38, v39
	v_exp_f32_e32 v57, v68
	v_pk_add_f32 v[32:33], v[66:67], v[32:33] neg_lo:[0,1] neg_hi:[0,1]
	v_cvt_pk_f16_f32 v68, v34, v35
	v_cvt_pk_f16_f32 v69, v32, v33
	v_cvt_f32_f16_e32 v32, v60
	v_cvt_f32_f16_sdwa v33, v60 dst_sel:DWORD dst_unused:UNUSED_PAD src0_sel:WORD_1
	v_cvt_f32_f16_e32 v34, v61
	v_cvt_f32_f16_sdwa v35, v61 dst_sel:DWORD dst_unused:UNUSED_PAD src0_sel:WORD_1
	v_mul_f32_e32 v64, 0x39b8aa3b, v64
	v_pk_add_f32 v[32:33], v[36:37], v[32:33] neg_lo:[0,1] neg_hi:[0,1]
	v_exp_f32_e32 v64, v64
	v_cvt_pk_f16_f32 v70, v32, v33
	v_pk_add_f32 v[32:33], v[38:39], v[34:35] neg_lo:[0,1] neg_hi:[0,1]
	v_cvt_f16_f32_e32 v62, v124
	v_cvt_pk_f16_f32 v71, v32, v33
	ds_read_b128 v[32:35], v120 offset:55296
	v_cvt_f16_f32_e32 v63, v125
	v_pk_mul_f32 v[30:31], v[64:65], v[30:31] op_sel_hi:[0,1]
	v_pk_mul_f32 v[28:29], v[64:65], v[28:29] op_sel_hi:[0,1]
	v_pk_mul_f32 v[26:27], v[64:65], v[26:27] op_sel_hi:[0,1]
	v_pk_mul_f32 v[24:25], v[64:65], v[24:25] op_sel_hi:[0,1]
	v_pk_mul_f32 v[22:23], v[64:65], v[22:23] op_sel_hi:[0,1]
	v_pk_mul_f32 v[20:21], v[64:65], v[20:21] op_sel_hi:[0,1]
	v_pk_mul_f32 v[18:19], v[64:65], v[18:19] op_sel_hi:[0,1]
	v_pk_mul_f32 v[16:17], v[64:65], v[16:17] op_sel_hi:[0,1]
	v_cvt_pk_f16_f32 v58, v65, v101
	v_cvt_f32_f16_e32 v62, v62
	v_cvt_f32_f16_e32 v75, v63
	s_waitcnt lgkmcnt(0)
	v_mfma_f32_32x32x16_f16 v[16:31], v[32:35], v[58:61], v[16:31]
	v_cvt_pk_f16_f32 v73, v40, v41
	v_sub_f32_e32 v74, v124, v62
	v_sub_f32_e32 v75, v125, v75
	v_cvt_f32_f16_e32 v62, v73
	v_cvt_f32_f16_sdwa v63, v73 dst_sel:DWORD dst_unused:UNUSED_PAD src0_sel:WORD_1
	v_cvt_pk_f16_f32 v76, v74, v75
	v_cvt_pk_f16_f32 v74, v42, v43
	v_cvt_f32_f16_e32 v78, v74
	v_cvt_f32_f16_sdwa v79, v74 dst_sel:DWORD dst_unused:UNUSED_PAD src0_sel:WORD_1
	v_cvt_pk_f16_f32 v75, v44, v45
	v_cvt_f32_f16_e32 v80, v75
	v_cvt_f32_f16_sdwa v81, v75 dst_sel:DWORD dst_unused:UNUSED_PAD src0_sel:WORD_1
	v_mfma_f32_32x32x16_f16 v[16:31], v[32:35], v[68:71], v[16:31]
	v_add_f32_e64 v62, v40, -v62
	v_add_f32_e64 v63, v41, -v63
	v_mul_f32_e64 v14, v64, v14
	v_mul_f32_e64 v15, v64, v15
	v_cvt_pk_f16_f32 v77, v62, v63
	v_pk_add_f32 v[62:63], v[42:43], v[78:79] neg_lo:[0,1] neg_hi:[0,1]
	v_pk_mul_f32 v[12:13], v[64:65], v[12:13] op_sel_hi:[0,1]
	v_cvt_pk_f16_f32 v78, v62, v63
	v_pk_add_f32 v[62:63], v[44:45], v[80:81] neg_lo:[0,1] neg_hi:[0,1]
	ds_read_b128 v[80:83], v120 offset:55328
	ds_read_b128 v[84:87], v120 offset:64512
	ds_read_b128 v[88:91], v120 offset:64544
	s_waitcnt lgkmcnt(1)
	v_mfma_f32_32x32x16_f16 v[16:31], v[84:87], v[58:61], v[16:31]
	ds_read_b128 v[92:95], v120 offset:59904
	ds_read_b128 v[96:99], v120 offset:59936
	v_cvt_pk_f16_f32 v79, v62, v63
	v_add_u32_e32 v63, 0xea20, v120
	v_cvt_f16_f32_e32 v62, v126
	ds_read_b128 v[108:111], v102 offset:9216
	ds_read_b128 v[112:115], v63 offset:9216
	v_cvt_f16_f32_e32 v63, v127
	v_pk_mul_f32 v[10:11], v[64:65], v[10:11] op_sel_hi:[0,1]
	v_pk_mul_f32 v[8:9], v[64:65], v[8:9] op_sel_hi:[0,1]
	v_pk_mul_f32 v[6:7], v[64:65], v[6:7] op_sel_hi:[0,1]
	v_pk_mul_f32 v[4:5], v[64:65], v[4:5] op_sel_hi:[0,1]
	v_pk_mul_f32 v[2:3], v[64:65], v[2:3] op_sel_hi:[0,1]
	v_pk_mul_f32 v[0:1], v[64:65], v[0:1] op_sel_hi:[0,1]
	v_cvt_pk_f16_f32 v33, v46, v47
	v_cvt_f32_f16_e32 v34, v33
	s_waitcnt lgkmcnt(3)
	v_mfma_f32_32x32x16_f16 v[0:15], v[92:95], v[58:61], v[0:15]
	v_cvt_f32_f16_sdwa v35, v33 dst_sel:DWORD dst_unused:UNUSED_PAD src0_sel:WORD_1
	v_cvt_pk_f16_f32 v72, v124, v125
	v_cvt_f32_f16_e32 v62, v62
	v_cvt_f32_f16_e32 v63, v63
	v_add_f32_e64 v34, v46, -v34
	v_add_f32_e64 v35, v47, -v35
	v_cvt_f16_f32_e32 v87, v128
	v_sub_f32_e32 v62, v126, v62
	v_mfma_f32_32x32x16_f16 v[16:31], v[80:83], v[72:75], v[16:31]
	v_sub_f32_e32 v63, v127, v63
	v_cvt_pk_f16_f32 v85, v34, v35
	v_cvt_pk_f16_f32 v34, v48, v49
	v_cvt_pk_f16_f32 v84, v62, v63
	v_cvt_f32_f16_e32 v62, v34
	v_cvt_f32_f16_sdwa v63, v34 dst_sel:DWORD dst_unused:UNUSED_PAD src0_sel:WORD_1
	v_cvt_pk_f16_f32 v35, v50, v51
	v_cvt_f32_f16_e32 v102, v35
	v_cvt_f32_f16_sdwa v103, v35 dst_sel:DWORD dst_unused:UNUSED_PAD src0_sel:WORD_1
	v_mfma_f32_32x32x16_f16 v[0:15], v[92:95], v[68:71], v[0:15]
	v_cvt_f16_f32_e32 v68, v129
	v_add_f32_e64 v62, v48, -v62
	v_add_f32_e64 v63, v49, -v63
	v_cvt_pk_f16_f32 v69, v52, v53
	v_cvt_pk_f16_f32 v86, v62, v63
	v_pk_add_f32 v[62:63], v[50:51], v[102:103] neg_lo:[0,1] neg_hi:[0,1]
	v_cvt_f32_f16_e32 v102, v87
	v_cvt_f32_f16_e32 v71, v68
	v_mfma_f32_32x32x16_f16 v[16:31], v[80:83], v[76:79], v[16:31]
	v_cvt_pk_f16_f32 v87, v62, v63
	v_cvt_f32_f16_e32 v62, v69
	v_cvt_f32_f16_sdwa v63, v69 dst_sel:DWORD dst_unused:UNUSED_PAD src0_sel:WORD_1
	v_sub_f32_e32 v70, v128, v102
	v_cvt_pk_f16_f32 v32, v126, v127
	v_add_u32_e32 v103, 0xea40, v120
	v_cvt_pk_f16_f32 v68, v128, v129
	s_waitcnt lgkmcnt(1)
	v_mfma_f32_32x32x16_f16 v[0:15], v[108:111], v[58:61], v[0:15]
	v_sub_f32_e32 v58, v129, v71
	v_cvt_pk_f16_f32 v58, v70, v58
	v_add_f32_e64 v60, v52, -v62
	v_add_f32_e64 v61, v53, -v63
	v_cvt_pk_f16_f32 v70, v54, v55
	v_cvt_pk_f16_f32 v71, v56, v57
	v_cvt_pk_f16_f32 v59, v60, v61
	v_cvt_f32_f16_e32 v60, v70
	v_cvt_f32_f16_sdwa v61, v70 dst_sel:DWORD dst_unused:UNUSED_PAD src0_sel:WORD_1
	v_cvt_f32_f16_e32 v62, v71
	v_cvt_f32_f16_sdwa v63, v71 dst_sel:DWORD dst_unused:UNUSED_PAD src0_sel:WORD_1
	v_mfma_f32_32x32x16_f16 v[16:31], v[88:91], v[72:75], v[16:31]
	v_add_f32_e64 v60, v54, -v60
	v_add_f32_e64 v61, v55, -v61
	ds_read_b128 v[80:83], v120 offset:55360
	ds_read_b128 v[92:95], v120 offset:55392
	ds_read_b128 v[108:111], v120 offset:64576
	ds_read_b128 v[116:119], v120 offset:64608
	v_pk_add_f32 v[62:63], v[56:57], v[62:63] neg_lo:[0,1] neg_hi:[0,1]
	v_cvt_pk_f16_f32 v60, v60, v61
	v_cvt_pk_f16_f32 v61, v62, v63
	v_add_f32_e32 v63, 0, v65
	v_add_f32_e32 v63, v63, v101
	v_add_f32_e32 v63, v63, v66
	v_add_f32_e32 v63, v63, v67
	v_add_f32_e32 v36, v63, v36
	s_waitcnt lgkmcnt(3)
	v_mfma_f32_32x32x16_f16 v[16:31], v[80:83], v[32:35], v[16:31]
	v_add_f32_e32 v36, v36, v37
	v_add_f32_e32 v36, v36, v38
	v_add_f32_e32 v36, v36, v39
	v_add_f32_e32 v36, v36, v124
	v_add_f32_e32 v36, v36, v125
	v_add_f32_e32 v36, v36, v40
	v_add_f32_e32 v36, v36, v41
	v_mfma_f32_32x32x16_f16 v[0:15], v[96:99], v[72:75], v[0:15]
	v_add_f32_e32 v36, v36, v42
	v_add_f32_e32 v36, v36, v43
	v_add_f32_e32 v36, v36, v44
	v_add_f32_e32 v36, v36, v45
	v_add_f32_e32 v36, v36, v126
	v_add_f32_e32 v36, v36, v127
	v_add_f32_e32 v36, v36, v46
	v_mfma_f32_32x32x16_f16 v[16:31], v[80:83], v[84:87], v[16:31]
	v_add_f32_e32 v36, v36, v47
	v_add_f32_e32 v36, v36, v48
	v_add_f32_e32 v36, v36, v49
	v_add_f32_e32 v36, v36, v50
	v_add_f32_e32 v36, v36, v51
	v_add_f32_e32 v36, v36, v128
	v_add_f32_e32 v36, v36, v129
	v_mfma_f32_32x32x16_f16 v[0:15], v[96:99], v[76:79], v[0:15]
	v_add_f32_e32 v36, v36, v52
	v_add_u32_e32 v62, 0xea60, v120
	ds_read_b128 v[88:91], v120 offset:59968
	ds_read_b128 v[120:123], v120 offset:60000
	v_add_f32_e32 v36, v36, v53
	v_add_f32_e32 v36, v36, v54
	v_add_f32_e32 v36, v36, v55
	v_add_f32_e32 v36, v36, v56
	s_waitcnt lgkmcnt(3)
	v_mfma_f32_32x32x16_f16 v[16:31], v[108:111], v[32:35], v[16:31]
	v_add_f32_e32 v44, v36, v57
	v_fmac_f32_e32 v44, v100, v64
	ds_bpermute_b32 v45, v107, v44
	ds_read_b128 v[36:39], v103 offset:9216
	ds_read_b128 v[40:43], v62 offset:9216
	s_waitcnt lgkmcnt(0)
	s_barrier
	v_mfma_f32_32x32x16_f16 v[0:15], v[112:115], v[72:75], v[0:15]
	v_add_f32_e32 v44, v44, v45
	v_div_scale_f32 v45, s[4:5], v44, v44, 4.0
	v_rcp_f32_e32 v46, v45
	s_nop 0
	v_fma_f32 v47, -v45, v46, 1.0
	v_mfma_f32_32x32x16_f16 v[16:31], v[92:95], v[68:71], v[16:31]
	v_fmac_f32_e32 v46, v47, v46
	v_div_scale_f32 v47, vcc, 4.0, v44, 4.0
	v_mul_f32_e32 v48, v47, v46
	v_fma_f32 v49, -v45, v48, v47
	v_fmac_f32_e32 v48, v49, v46
	v_fma_f32 v45, -v45, v48, v47
	v_mfma_f32_32x32x16_f16 v[0:15], v[88:91], v[32:35], v[0:15]
	v_div_fmas_f32 v45, v45, v46, v48
	v_div_fixup_f32 v44, v45, v44, 4.0
	v_or3_b32 v47, s1, 0, 0
	v_or3_b32 v46, s0, v106, v104
	s_lshl_b32 s0, s2, 7
	v_lshlrev_b64 v[46:47], 10, v[46:47]
	s_and_b32 s0, s0, 0x380
	v_mfma_f32_32x32x16_f16 v[16:31], v[92:95], v[58:61], v[16:31]
	v_or_b32_e32 v46, s0, v46
	v_lshl_add_u64 v[48:49], s[8:9], 0, v[46:47]
	v_lshl_add_u64 v[46:47], s[10:11], 0, v[46:47]
	v_mfma_f32_32x32x16_f16 v[0:15], v[88:91], v[84:87], v[0:15]
	v_mfma_f32_32x32x16_f16 v[16:31], v[116:119], v[68:71], v[16:31]
	v_mfma_f32_32x32x16_f16 v[0:15], v[36:39], v[32:35], v[0:15]
	s_nop 10
	v_mul_f32_e32 v45, v44, v16
	v_fma_mixlo_f16 v50, v44, v16, 0
	v_fma_mixlo_f16 v16, v44, v16, -v50 op_sel_hi:[0,0,1]
	v_mul_f32_e64 v50, v44, v18
	v_mul_f32_e64 v51, v44, v19
	v_cvt_pk_f16_f32 v51, v50, v51
	v_cvt_f32_f16_e32 v52, v51
	v_cvt_f32_f16_sdwa v53, v51 dst_sel:DWORD dst_unused:UNUSED_PAD src0_sel:WORD_1
	v_mfma_f32_32x32x16_f16 v[0:15], v[120:123], v[68:71], v[0:15]
	v_mul_f32_e64 v32, v44, v22
	v_mul_f32_e64 v33, v44, v23
	v_fma_mixlo_f16 v55, v44, v17, 0
	v_fma_f32 v18, v44, v18, -v52
	v_fma_f32 v19, v44, v19, -v53
	v_cvt_pk_f16_f32 v33, v32, v33
	v_mul_f32_e32 v54, v44, v17
	v_fma_mixhi_f16 v16, v44, v17, -v55 op_sel_hi:[0,0,1]
	v_cvt_pk_f16_f32 v17, v18, v19
	v_lshlrev_b32_e32 v18, 3, v105
	v_mov_b32_e32 v19, 0
	v_cvt_f32_f16_e32 v34, v33
	v_cvt_f32_f16_sdwa v35, v33 dst_sel:DWORD dst_unused:UNUSED_PAD src0_sel:WORD_1
	v_lshl_add_u64 v[48:49], v[48:49], 0, v[18:19]
	v_lshl_add_u64 v[18:19], v[46:47], 0, v[18:19]
	global_store_dwordx2 v[18:19], v[16:17], off
	v_fma_mixlo_f16 v16, v44, v20, 0
	v_mul_f32_e32 v17, v44, v20
	v_fma_mixlo_f16 v16, v44, v20, -v16 op_sel_hi:[0,0,1]
	v_mul_f32_e32 v20, v44, v21
	v_fma_mixlo_f16 v36, v44, v21, 0
	v_mfma_f32_32x32x16_f16 v[0:15], v[120:123], v[58:61], v[0:15]
	v_cvt_pk_f16_f32 v32, v17, v20
	v_fma_mixhi_f16 v16, v44, v21, -v36 op_sel_hi:[0,0,1]
	v_fma_f32 v20, v44, v22, -v34
	v_fma_f32 v21, v44, v23, -v35
	v_cvt_pk_f16_f32 v17, v20, v21
	v_pk_mul_f32 v[20:21], v[44:45], v[26:27] op_sel_hi:[0,1]
	v_cvt_pk_f16_f32 v21, v20, v21
	v_cvt_f32_f16_e32 v22, v21
	v_cvt_f32_f16_sdwa v23, v21 dst_sel:DWORD dst_unused:UNUSED_PAD src0_sel:WORD_1
	v_cvt_pk_f16_f32 v50, v45, v54
	global_store_dwordx2 v[48:49], v[50:51], off
	global_store_dwordx2 v[48:49], v[32:33], off offset:16
	global_store_dwordx2 v[18:19], v[16:17], off offset:16
	v_fma_mixlo_f16 v16, v44, v24, 0
	v_mul_f32_e32 v17, v44, v24
	v_fma_mixlo_f16 v16, v44, v24, -v16 op_sel_hi:[0,0,1]
	v_mul_f32_e32 v24, v44, v25
	v_mfma_f32_32x32x16_f16 v[0:15], v[40:43], v[68:71], v[0:15]
	v_fma_mixlo_f16 v32, v44, v25, 0
	v_cvt_pk_f16_f32 v20, v17, v24
	v_fma_f32 v22, v44, v26, -v22
	v_fma_f32 v23, v44, v27, -v23
	v_fma_mixhi_f16 v16, v44, v25, -v32 op_sel_hi:[0,0,1]
	v_cvt_pk_f16_f32 v17, v22, v23
	global_store_dwordx2 v[48:49], v[20:21], off offset:32
	global_store_dwordx2 v[18:19], v[16:17], off offset:32
	v_pk_mul_f32 v[20:21], v[44:45], v[30:31] op_sel_hi:[0,1]
	v_cvt_pk_f16_f32 v21, v20, v21
	v_cvt_f32_f16_e32 v22, v21
	v_cvt_f32_f16_sdwa v23, v21 dst_sel:DWORD dst_unused:UNUSED_PAD src0_sel:WORD_1
	v_fma_mixlo_f16 v16, v44, v28, 0
	v_mul_f32_e32 v17, v44, v28
	v_fma_mixlo_f16 v16, v44, v28, -v16 op_sel_hi:[0,0,1]
	v_mul_f32_e32 v24, v44, v29
	v_fma_mixlo_f16 v25, v44, v29, 0
	v_cvt_pk_f16_f32 v20, v17, v24
	v_fma_mixhi_f16 v16, v44, v29, -v25 op_sel_hi:[0,0,1]
	v_pk_fma_f32 v[22:23], v[44:45], v[30:31], v[22:23] op_sel_hi:[0,1,1] neg_lo:[0,0,1] neg_hi:[0,0,1]
	v_cvt_pk_f16_f32 v17, v22, v23
	global_store_dwordx2 v[48:49], v[20:21], off offset:48
	global_store_dwordx2 v[18:19], v[16:17], off offset:48
	v_fma_mixlo_f16 v16, v44, v0, 0
	v_mul_f32_e32 v22, v44, v0
	v_fma_mixlo_f16 v0, v44, v0, -v16 op_sel_hi:[0,0,1]
	v_pk_mul_f32 v[16:17], v[44:45], v[2:3] op_sel_hi:[0,1]
	v_cvt_pk_f16_f32 v17, v16, v17
	v_cvt_f32_f16_e32 v20, v17
	v_cvt_f32_f16_sdwa v21, v17 dst_sel:DWORD dst_unused:UNUSED_PAD src0_sel:WORD_1
	v_fma_mixlo_f16 v24, v44, v1, 0
	v_mul_f32_e32 v23, v44, v1
	v_fma_mixhi_f16 v0, v44, v1, -v24 op_sel_hi:[0,0,1]
	v_pk_fma_f32 v[2:3], v[44:45], v[2:3], v[20:21] op_sel_hi:[0,1,1] neg_lo:[0,0,1] neg_hi:[0,0,1]
	v_cvt_pk_f16_f32 v1, v2, v3
	v_pk_mul_f32 v[2:3], v[44:45], v[6:7] op_sel_hi:[0,1]
	v_cvt_pk_f16_f32 v16, v22, v23
	v_cvt_pk_f16_f32 v3, v2, v3
	global_store_dwordx2 v[48:49], v[16:17], off offset:64
	global_store_dwordx2 v[18:19], v[0:1], off offset:64
	v_cvt_f32_f16_e32 v16, v3
	v_cvt_f32_f16_sdwa v17, v3 dst_sel:DWORD dst_unused:UNUSED_PAD src0_sel:WORD_1
	v_fma_mixlo_f16 v0, v44, v4, 0
	v_mul_f32_e32 v1, v44, v4
	v_fma_mixlo_f16 v0, v44, v4, -v0 op_sel_hi:[0,0,1]
	v_mul_f32_e32 v4, v44, v5
	v_fma_mixlo_f16 v20, v44, v5, 0
	v_cvt_pk_f16_f32 v2, v1, v4
	v_fma_mixhi_f16 v0, v44, v5, -v20 op_sel_hi:[0,0,1]
	v_pk_fma_f32 v[4:5], v[44:45], v[6:7], v[16:17] op_sel_hi:[0,1,1] neg_lo:[0,0,1] neg_hi:[0,0,1]
	v_cvt_pk_f16_f32 v1, v4, v5
	global_store_dwordx2 v[48:49], v[2:3], off offset:80
	global_store_dwordx2 v[18:19], v[0:1], off offset:80
	v_pk_mul_f32 v[2:3], v[44:45], v[10:11] op_sel_hi:[0,1]
	v_cvt_pk_f16_f32 v3, v2, v3
	v_cvt_f32_f16_e32 v4, v3
	v_cvt_f32_f16_sdwa v5, v3 dst_sel:DWORD dst_unused:UNUSED_PAD src0_sel:WORD_1
	v_mul_f32_e32 v1, v44, v8
	v_fma_mixlo_f16 v0, v44, v8, 0
	v_mul_f32_e32 v6, v44, v9
	v_fma_mixlo_f16 v0, v44, v8, -v0 op_sel_hi:[0,0,1]
	v_fma_mixlo_f16 v7, v44, v9, 0
	v_cvt_pk_f16_f32 v2, v1, v6
	v_pk_fma_f32 v[4:5], v[44:45], v[10:11], v[4:5] op_sel_hi:[0,1,1] neg_lo:[0,0,1] neg_hi:[0,0,1]
	v_fma_mixhi_f16 v0, v44, v9, -v7 op_sel_hi:[0,0,1]
	v_cvt_pk_f16_f32 v1, v4, v5
	global_store_dwordx2 v[48:49], v[2:3], off offset:96
	global_store_dwordx2 v[18:19], v[0:1], off offset:96
	v_pk_mul_f32 v[2:3], v[44:45], v[14:15] op_sel_hi:[0,1]
	v_cvt_pk_f16_f32 v3, v2, v3
	v_cvt_f32_f16_e32 v4, v3
	v_cvt_f32_f16_sdwa v5, v3 dst_sel:DWORD dst_unused:UNUSED_PAD src0_sel:WORD_1
	v_mul_f32_e32 v1, v44, v12
	v_fma_mixlo_f16 v0, v44, v12, 0
	v_mul_f32_e32 v6, v44, v13
	v_fma_mixlo_f16 v0, v44, v12, -v0 op_sel_hi:[0,0,1]
	v_fma_mixlo_f16 v7, v44, v13, 0
	v_cvt_pk_f16_f32 v2, v1, v6
	v_pk_fma_f32 v[4:5], v[44:45], v[14:15], v[4:5] op_sel_hi:[0,1,1] neg_lo:[0,0,1] neg_hi:[0,0,1]
	v_fma_mixhi_f16 v0, v44, v13, -v7 op_sel_hi:[0,0,1]
	v_cvt_pk_f16_f32 v1, v4, v5
	global_store_dwordx2 v[48:49], v[2:3], off offset:112
	global_store_dwordx2 v[18:19], v[0:1], off offset:112
	s_endpgm
	.p2alignl 8, 3212836864
